# GEMM bf16 epilogues: next piece conversions and its two LDS writes issued before the wait for this piece's LDS read-back (lgkmcnt(2) instead of lgkmcnt(0) right behind the reads); on top of e1
# speedup vs baseline: 1.0031x; 1.0031x over previous
.LBB0_404:
	s_lshl_b32 s20, s70, 8
	v_lshl_add_u32 v149, s71, 8, v143
	v_mov_b64_e32 v[150:151], s[50:51]
	v_cvt_pk_bf16_f32 v124, v124, v125
	v_cvt_pk_bf16_f32 v125, v126, v127
	v_cvt_pk_bf16_f32 v126, v120, v121
	v_cvt_pk_bf16_f32 v127, v122, v123
	v_cvt_pk_bf16_f32 v108, v108, v109
	v_cvt_pk_bf16_f32 v109, v110, v111
	v_cvt_pk_bf16_f32 v110, v104, v105
	v_cvt_pk_bf16_f32 v111, v106, v107
	v_mad_i64_i32 v[150:151], s[30:31], v149, s3, v[150:151]
	s_ashr_i32 s21, s20, 31
	ds_write_b128 v141, v[124:127]
	ds_write_b128 v147, v[108:111]
	v_lshl_add_u64 v[150:151], s[20:21], 1, v[150:151]
	ds_read_b128 v[104:107], v148 offset:1024
	ds_read_b128 v[108:111], v142
	v_lshl_add_u64 v[150:151], v[150:151], 0, s[80:81]
	v_lshl_add_u64 v[150:151], v[150:151], 0, v[160:161]
	s_mov_b32 s13, 0x18000
	v_cvt_pk_bf16_f32 v92, v92, v93
	v_cvt_pk_bf16_f32 v93, v94, v95
	v_cvt_pk_bf16_f32 v94, v88, v89
	v_add_co_u32_e32 v88, vcc, s13, v150
	v_cvt_pk_bf16_f32 v116, v116, v117
	v_cvt_pk_bf16_f32 v117, v118, v119
	v_cvt_pk_bf16_f32 v118, v112, v113
	v_cvt_pk_bf16_f32 v119, v114, v115
	v_cvt_pk_bf16_f32 v95, v90, v91
	v_addc_co_u32_e32 v89, vcc, 0, v151, vcc
	ds_write_b128 v141, v[116:119]
	ds_write_b128 v147, v[92:95]
	s_waitcnt lgkmcnt(0)
	global_store_dwordx4 v[150:151], v[108:111], off nt
	global_store_dwordx4 v[88:89], v[104:107], off nt
	ds_read_b128 v[88:91], v142
	ds_read_b128 v[92:95], v148 offset:1024
	v_cvt_pk_bf16_f32 v80, v80, v81
	v_cvt_pk_bf16_f32 v81, v82, v83
	v_cvt_pk_bf16_f32 v82, v72, v73
	v_add_co_u32_e32 v72, vcc, s74, v150
	s_mov_b32 s13, 0x48000
	s_nop 0
	v_addc_co_u32_e32 v73, vcc, 0, v151, vcc
	v_cvt_pk_bf16_f32 v100, v100, v101
	v_cvt_pk_bf16_f32 v101, v102, v103
	v_cvt_pk_bf16_f32 v102, v96, v97
	v_cvt_pk_bf16_f32 v103, v98, v99
	v_cvt_pk_bf16_f32 v83, v74, v75
	ds_write_b128 v141, v[100:103]
	ds_write_b128 v147, v[80:83]
	s_waitcnt lgkmcnt(2)
	global_store_dwordx4 v[72:73], v[88:91], off nt
	v_add_co_u32_e32 v72, vcc, s13, v150
	s_nop 1
	v_addc_co_u32_e32 v73, vcc, 0, v151, vcc
	global_store_dwordx4 v[72:73], v[92:95], off nt
	ds_read_b128 v[72:75], v142
	ds_read_b128 v[80:83], v148 offset:1024
	s_mov_b32 s13, 0x60000
	v_cvt_pk_bf16_f32 v68, v68, v69
	v_cvt_pk_bf16_f32 v69, v70, v71
	v_cvt_pk_bf16_f32 v70, v64, v65
	v_add_co_u32_e32 v64, vcc, s13, v150
	s_mov_b32 s13, 0x78000
	s_nop 0
	v_addc_co_u32_e32 v65, vcc, 0, v151, vcc
	v_cvt_pk_bf16_f32 v84, v84, v85
	v_cvt_pk_bf16_f32 v85, v86, v87
	v_cvt_pk_bf16_f32 v86, v76, v77
	v_cvt_pk_bf16_f32 v87, v78, v79
	v_cvt_pk_bf16_f32 v71, v66, v67
	ds_write_b128 v141, v[84:87]
	ds_write_b128 v147, v[68:71]
	s_waitcnt lgkmcnt(2)
	global_store_dwordx4 v[64:65], v[72:75], off nt
	v_add_co_u32_e32 v64, vcc, s13, v150
	s_nop 1
	v_addc_co_u32_e32 v65, vcc, 0, v151, vcc
	global_store_dwordx4 v[64:65], v[80:83], off nt
	ds_read_b128 v[64:67], v142
	ds_read_b128 v[68:71], v148 offset:1024
	v_cvt_pk_bf16_f32 v48, v48, v49
	v_cvt_pk_bf16_f32 v49, v50, v51
	v_cvt_pk_bf16_f32 v50, v40, v41
	v_add_co_u32_e32 v40, vcc, s0, v150
	s_mov_b32 s13, 0xa8000
	s_nop 0
	v_addc_co_u32_e32 v41, vcc, 0, v151, vcc
	v_cvt_pk_bf16_f32 v60, v60, v61
	v_cvt_pk_bf16_f32 v61, v62, v63
	v_cvt_pk_bf16_f32 v62, v56, v57
	v_cvt_pk_bf16_f32 v63, v58, v59
	v_cvt_pk_bf16_f32 v51, v42, v43
	ds_write_b128 v141, v[60:63]
	ds_write_b128 v147, v[48:51]
	s_waitcnt lgkmcnt(2)
	global_store_dwordx4 v[40:41], v[64:67], off nt
	v_add_co_u32_e32 v40, vcc, s13, v150
	s_nop 1
	v_addc_co_u32_e32 v41, vcc, 0, v151, vcc
	global_store_dwordx4 v[40:41], v[68:71], off nt
	ds_read_b128 v[40:43], v142
	ds_read_b128 v[48:51], v148 offset:1024
	s_mov_b32 s13, 0x180000
	v_cvt_pk_bf16_f32 v32, v32, v33
	v_cvt_pk_bf16_f32 v33, v34, v35
	v_cvt_pk_bf16_f32 v34, v24, v25
	v_add_co_u32_e32 v24, vcc, s13, v150
	s_mov_b32 s13, 0x198000
	s_nop 0
	v_addc_co_u32_e32 v25, vcc, 0, v151, vcc
	v_cvt_pk_bf16_f32 v52, v52, v53
	v_cvt_pk_bf16_f32 v53, v54, v55
	v_cvt_pk_bf16_f32 v54, v44, v45
	v_cvt_pk_bf16_f32 v55, v46, v47
	v_cvt_pk_bf16_f32 v35, v26, v27
	ds_write_b128 v141, v[52:55]
	ds_write_b128 v147, v[32:35]
	s_waitcnt lgkmcnt(2)
	global_store_dwordx4 v[24:25], v[40:43], off nt
	v_add_co_u32_e32 v24, vcc, s13, v150
	s_nop 1
	v_addc_co_u32_e32 v25, vcc, 0, v151, vcc
	global_store_dwordx4 v[24:25], v[48:51], off nt
	ds_read_b128 v[24:27], v142
	ds_read_b128 v[32:35], v148 offset:1024
	s_mov_b32 s13, 0x1b0000
	v_cvt_pk_bf16_f32 v16, v16, v17
	v_cvt_pk_bf16_f32 v17, v18, v19
	v_cvt_pk_bf16_f32 v18, v8, v9
	v_add_co_u32_e32 v8, vcc, s13, v150
	s_mov_b32 s13, 0x1c8000
	s_nop 0
	v_addc_co_u32_e32 v9, vcc, 0, v151, vcc
	v_cvt_pk_bf16_f32 v36, v36, v37
	v_cvt_pk_bf16_f32 v37, v38, v39
	v_cvt_pk_bf16_f32 v38, v28, v29
	v_cvt_pk_bf16_f32 v39, v30, v31
	v_cvt_pk_bf16_f32 v19, v10, v11
	ds_write_b128 v141, v[36:39]
	ds_write_b128 v147, v[16:19]
	s_waitcnt lgkmcnt(2)
	global_store_dwordx4 v[8:9], v[24:27], off nt
	v_add_co_u32_e32 v8, vcc, s13, v150
	s_nop 1
	v_addc_co_u32_e32 v9, vcc, 0, v151, vcc
	global_store_dwordx4 v[8:9], v[32:35], off nt
	ds_read_b128 v[8:11], v142
	ds_read_b128 v[16:19], v148 offset:1024
	s_mov_b32 s13, 0x1e0000
	v_cvt_pk_bf16_f32 v4, v4, v5
	v_cvt_pk_bf16_f32 v5, v6, v7
	v_cvt_pk_bf16_f32 v6, v0, v1
	v_add_co_u32_e32 v0, vcc, s13, v150
	s_mov_b32 s13, 0x1f8000
	s_nop 0
	v_addc_co_u32_e32 v1, vcc, 0, v151, vcc
	v_cvt_pk_bf16_f32 v20, v20, v21
	v_cvt_pk_bf16_f32 v21, v22, v23
	v_cvt_pk_bf16_f32 v22, v12, v13
	v_cvt_pk_bf16_f32 v23, v14, v15
	v_cvt_pk_bf16_f32 v7, v2, v3
	ds_write_b128 v141, v[20:23]
	ds_write_b128 v147, v[4:7]
	s_waitcnt lgkmcnt(2)
	global_store_dwordx4 v[0:1], v[8:11], off nt
	v_add_co_u32_e32 v0, vcc, s13, v150
	s_nop 1
	v_addc_co_u32_e32 v1, vcc, 0, v151, vcc
	global_store_dwordx4 v[0:1], v[16:19], off nt
	ds_read_b128 v[0:3], v142
	ds_read_b128 v[4:7], v148 offset:1024
	v_add_co_u32_e32 v8, vcc, 0x210000, v150
	s_mov_b32 s90, 0x3fb8aa3b
	s_nop 0
	v_addc_co_u32_e32 v9, vcc, 0, v151, vcc
	s_waitcnt lgkmcnt(0)
	global_store_dwordx4 v[8:9], v[0:3], off nt
	s_nop 1
	v_add_co_u32_e32 v0, vcc, 0x228000, v150
	s_nop 1
	v_addc_co_u32_e32 v1, vcc, 0, v151, vcc
	s_andn2_b64 vcc, exec, s[8:9]
	s_mov_b64 s[8:9], -1
	global_store_dwordx4 v[0:1], v[4:7], off nt
	s_cbranch_vccnz .LBB0_397
	s_andn2_b64 vcc, exec, s[4:5]
	s_cbranch_vccnz .LBB0_396
	s_barrier
	s_branch .LBB0_396

.LBB0_504:
	v_lshl_add_u32 v150, s73, 8, v143
	v_ashrrev_i32_e32 v151, 31, v150
	s_lshl_b32 s30, s72, 8
	v_lshlrev_b64 v[150:151], 12, v[150:151]
	v_cvt_pk_bf16_f32 v124, v124, v125
	v_cvt_pk_bf16_f32 v125, v126, v127
	v_cvt_pk_bf16_f32 v126, v120, v121
	v_cvt_pk_bf16_f32 v127, v122, v123
	v_cvt_pk_bf16_f32 v108, v108, v109
	v_cvt_pk_bf16_f32 v109, v110, v111
	v_cvt_pk_bf16_f32 v110, v104, v105
	v_cvt_pk_bf16_f32 v111, v106, v107
	v_lshl_add_u64 v[150:151], s[50:51], 0, v[150:151]
	s_ashr_i32 s31, s30, 31
	ds_write_b128 v141, v[124:127]
	ds_write_b128 v147, v[108:111]
	v_lshl_add_u64 v[150:151], s[30:31], 1, v[150:151]
	ds_read_b128 v[104:107], v148 offset:1024
	ds_read_b128 v[108:111], v142
	v_lshl_add_u64 v[150:151], v[150:151], 0, s[80:81]
	v_lshl_add_u64 v[150:151], v[150:151], 0, v[160:161]
	v_cvt_pk_bf16_f32 v92, v92, v93
	v_cvt_pk_bf16_f32 v93, v94, v95
	v_cvt_pk_bf16_f32 v94, v88, v89
	v_add_co_u32_e32 v88, vcc, s97, v150
	v_cvt_pk_bf16_f32 v116, v116, v117
	v_cvt_pk_bf16_f32 v117, v118, v119
	v_cvt_pk_bf16_f32 v118, v112, v113
	v_cvt_pk_bf16_f32 v119, v114, v115
	v_cvt_pk_bf16_f32 v95, v90, v91
	v_addc_co_u32_e32 v89, vcc, 0, v151, vcc
	ds_write_b128 v141, v[116:119]
	ds_write_b128 v147, v[92:95]
	s_waitcnt lgkmcnt(0)
	global_store_dwordx4 v[150:151], v[108:111], off nt
	global_store_dwordx4 v[88:89], v[104:107], off nt
	ds_read_b128 v[88:91], v142
	ds_read_b128 v[92:95], v148 offset:1024
	v_cvt_pk_bf16_f32 v80, v80, v81
	v_cvt_pk_bf16_f32 v81, v82, v83
	v_cvt_pk_bf16_f32 v82, v72, v73
	v_add_co_u32_e32 v72, vcc, s96, v150
	s_mov_b32 s15, 0x18000
	s_nop 0
	v_addc_co_u32_e32 v73, vcc, 0, v151, vcc
	v_cvt_pk_bf16_f32 v100, v100, v101
	v_cvt_pk_bf16_f32 v101, v102, v103
	v_cvt_pk_bf16_f32 v102, v96, v97
	v_cvt_pk_bf16_f32 v103, v98, v99
	v_cvt_pk_bf16_f32 v83, v74, v75
	ds_write_b128 v141, v[100:103]
	ds_write_b128 v147, v[80:83]
	s_waitcnt lgkmcnt(2)
	global_store_dwordx4 v[72:73], v[88:91], off nt
	v_add_co_u32_e32 v72, vcc, s15, v150
	s_nop 1
	v_addc_co_u32_e32 v73, vcc, 0, v151, vcc
	global_store_dwordx4 v[72:73], v[92:95], off nt
	ds_read_b128 v[72:75], v142
	ds_read_b128 v[80:83], v148 offset:1024
	v_cvt_pk_bf16_f32 v68, v68, v69
	v_cvt_pk_bf16_f32 v69, v70, v71
	v_cvt_pk_bf16_f32 v70, v64, v65
	v_add_co_u32_e32 v64, vcc, s92, v150
	s_mov_b32 s15, 0x28000
	s_nop 0
	v_addc_co_u32_e32 v65, vcc, 0, v151, vcc
	v_cvt_pk_bf16_f32 v84, v84, v85
	v_cvt_pk_bf16_f32 v85, v86, v87
	v_cvt_pk_bf16_f32 v86, v76, v77
	v_cvt_pk_bf16_f32 v87, v78, v79
	v_cvt_pk_bf16_f32 v71, v66, v67
	ds_write_b128 v141, v[84:87]
	ds_write_b128 v147, v[68:71]
	s_waitcnt lgkmcnt(2)
	global_store_dwordx4 v[64:65], v[72:75], off nt
	v_add_co_u32_e32 v64, vcc, s15, v150
	s_nop 1
	v_addc_co_u32_e32 v65, vcc, 0, v151, vcc
	global_store_dwordx4 v[64:65], v[80:83], off nt
	ds_read_b128 v[64:67], v142
	ds_read_b128 v[68:71], v148 offset:1024
	v_cvt_pk_bf16_f32 v48, v48, v49
	v_cvt_pk_bf16_f32 v49, v50, v51
	v_cvt_pk_bf16_f32 v50, v40, v41
	v_add_co_u32_e32 v40, vcc, s74, v150
	s_mov_b32 s15, 0x38000
	s_nop 0
	v_addc_co_u32_e32 v41, vcc, 0, v151, vcc
	v_cvt_pk_bf16_f32 v60, v60, v61
	v_cvt_pk_bf16_f32 v61, v62, v63
	v_cvt_pk_bf16_f32 v62, v56, v57
	v_cvt_pk_bf16_f32 v63, v58, v59
	v_cvt_pk_bf16_f32 v51, v42, v43
	ds_write_b128 v141, v[60:63]
	ds_write_b128 v147, v[48:51]
	s_waitcnt lgkmcnt(2)
	global_store_dwordx4 v[40:41], v[64:67], off nt
	v_add_co_u32_e32 v40, vcc, s15, v150
	s_nop 1
	v_addc_co_u32_e32 v41, vcc, 0, v151, vcc
	global_store_dwordx4 v[40:41], v[68:71], off nt
	ds_read_b128 v[40:43], v142
	ds_read_b128 v[48:51], v148 offset:1024
	v_cvt_pk_bf16_f32 v32, v32, v33
	v_cvt_pk_bf16_f32 v33, v34, v35
	v_cvt_pk_bf16_f32 v34, v24, v25
	v_add_co_u32_e32 v24, vcc, s61, v150
	s_mov_b32 s15, 0x88000
	s_nop 0
	v_addc_co_u32_e32 v25, vcc, 0, v151, vcc
	v_cvt_pk_bf16_f32 v52, v52, v53
	v_cvt_pk_bf16_f32 v53, v54, v55
	v_cvt_pk_bf16_f32 v54, v44, v45
	v_cvt_pk_bf16_f32 v55, v46, v47
	v_cvt_pk_bf16_f32 v35, v26, v27
	ds_write_b128 v141, v[52:55]
	ds_write_b128 v147, v[32:35]
	s_waitcnt lgkmcnt(2)
	global_store_dwordx4 v[24:25], v[40:43], off nt
	v_add_co_u32_e32 v24, vcc, s15, v150
	s_nop 1
	v_addc_co_u32_e32 v25, vcc, 0, v151, vcc
	global_store_dwordx4 v[24:25], v[48:51], off nt
	ds_read_b128 v[24:27], v142
	ds_read_b128 v[32:35], v148 offset:1024
	v_cvt_pk_bf16_f32 v16, v16, v17
	v_cvt_pk_bf16_f32 v17, v18, v19
	v_cvt_pk_bf16_f32 v18, v8, v9
	v_add_co_u32_e32 v8, vcc, s0, v150
	s_mov_b32 s15, 0x98000
	s_nop 0
	v_addc_co_u32_e32 v9, vcc, 0, v151, vcc
	v_cvt_pk_bf16_f32 v36, v36, v37
	v_cvt_pk_bf16_f32 v37, v38, v39
	v_cvt_pk_bf16_f32 v38, v28, v29
	v_cvt_pk_bf16_f32 v39, v30, v31
	v_cvt_pk_bf16_f32 v19, v10, v11
	ds_write_b128 v141, v[36:39]
	ds_write_b128 v147, v[16:19]
	s_waitcnt lgkmcnt(2)
	global_store_dwordx4 v[8:9], v[24:27], off nt
	v_add_co_u32_e32 v8, vcc, s15, v150
	s_nop 1
	v_addc_co_u32_e32 v9, vcc, 0, v151, vcc
	global_store_dwordx4 v[8:9], v[32:35], off nt
	ds_read_b128 v[8:11], v142
	ds_read_b128 v[16:19], v148 offset:1024
	v_cvt_pk_bf16_f32 v4, v4, v5
	v_cvt_pk_bf16_f32 v5, v6, v7
	v_cvt_pk_bf16_f32 v6, v0, v1
	v_add_co_u32_e32 v0, vcc, s85, v150
	s_mov_b32 s15, 0xa8000
	s_nop 0
	v_addc_co_u32_e32 v1, vcc, 0, v151, vcc
	v_cvt_pk_bf16_f32 v20, v20, v21
	v_cvt_pk_bf16_f32 v21, v22, v23
	v_cvt_pk_bf16_f32 v22, v12, v13
	v_cvt_pk_bf16_f32 v23, v14, v15
	v_cvt_pk_bf16_f32 v7, v2, v3
	ds_write_b128 v141, v[20:23]
	ds_write_b128 v147, v[4:7]
	s_waitcnt lgkmcnt(2)
	global_store_dwordx4 v[0:1], v[8:11], off nt
	v_add_co_u32_e32 v0, vcc, s15, v150
	s_nop 1
	v_addc_co_u32_e32 v1, vcc, 0, v151, vcc
	global_store_dwordx4 v[0:1], v[16:19], off nt
	ds_read_b128 v[0:3], v142
	ds_read_b128 v[4:7], v148 offset:1024
	v_add_co_u32_e32 v8, vcc, 0xb0000, v150
	s_mov_b32 s90, 0x3fb8aa3b
	s_nop 0
	v_addc_co_u32_e32 v9, vcc, 0, v151, vcc
	s_waitcnt lgkmcnt(0)
	global_store_dwordx4 v[8:9], v[0:3], off nt
	s_nop 1
	v_add_co_u32_e32 v0, vcc, 0xb8000, v150
	s_nop 1
	v_addc_co_u32_e32 v1, vcc, 0, v151, vcc
	s_andn2_b64 vcc, exec, s[8:9]
	s_mov_b64 s[8:9], -1
	global_store_dwordx4 v[0:1], v[4:7], off nt
	s_cbranch_vccnz .LBB0_497
	s_andn2_b64 vcc, exec, s[10:11]
	s_cbranch_vccnz .LBB0_496
	s_barrier
	s_branch .LBB0_496

.LBB0_859:
	v_lshl_add_u32 v150, s59, 8, v143
	v_ashrrev_i32_e32 v151, 31, v150
	s_lshl_b32 s18, s58, 8
	v_lshlrev_b64 v[150:151], 13, v[150:151]
	v_cvt_pk_bf16_f32 v124, v124, v125
	v_cvt_pk_bf16_f32 v125, v126, v127
	v_cvt_pk_bf16_f32 v126, v120, v121
	v_cvt_pk_bf16_f32 v127, v122, v123
	v_cvt_pk_bf16_f32 v108, v108, v109
	v_cvt_pk_bf16_f32 v109, v110, v111
	v_cvt_pk_bf16_f32 v110, v104, v105
	v_cvt_pk_bf16_f32 v111, v106, v107
	v_lshl_add_u64 v[150:151], s[52:53], 0, v[150:151]
	s_ashr_i32 s19, s18, 31
	ds_write_b128 v141, v[124:127]
	ds_write_b128 v147, v[108:111]
	v_lshl_add_u64 v[150:151], s[18:19], 1, v[150:151]
	ds_read_b128 v[104:107], v148 offset:1024
	ds_read_b128 v[108:111], v142
	v_lshl_add_u64 v[150:151], v[150:151], 0, s[80:81]
	v_lshl_add_u64 v[150:151], v[150:151], 0, v[160:161]
	v_cvt_pk_bf16_f32 v92, v92, v93
	v_cvt_pk_bf16_f32 v93, v94, v95
	v_cvt_pk_bf16_f32 v94, v88, v89
	v_add_co_u32_e32 v88, vcc, s96, v150
	v_cvt_pk_bf16_f32 v116, v116, v117
	v_cvt_pk_bf16_f32 v117, v118, v119
	v_cvt_pk_bf16_f32 v118, v112, v113
	v_cvt_pk_bf16_f32 v119, v114, v115
	v_cvt_pk_bf16_f32 v95, v90, v91
	v_addc_co_u32_e32 v89, vcc, 0, v151, vcc
	ds_write_b128 v141, v[116:119]
	ds_write_b128 v147, v[92:95]
	s_waitcnt lgkmcnt(0)
	global_store_dwordx4 v[150:151], v[108:111], off nt
	global_store_dwordx4 v[88:89], v[104:107], off nt
	ds_read_b128 v[88:91], v142
	ds_read_b128 v[92:95], v148 offset:1024
	v_cvt_pk_bf16_f32 v80, v80, v81
	v_cvt_pk_bf16_f32 v81, v82, v83
	v_cvt_pk_bf16_f32 v82, v72, v73
	v_add_co_u32_e32 v72, vcc, s92, v150
	v_cvt_pk_bf16_f32 v100, v100, v101
	s_nop 0
	v_addc_co_u32_e32 v73, vcc, 0, v151, vcc
	v_cvt_pk_bf16_f32 v101, v102, v103
	v_cvt_pk_bf16_f32 v102, v96, v97
	v_cvt_pk_bf16_f32 v103, v98, v99
	v_cvt_pk_bf16_f32 v83, v74, v75
	ds_write_b128 v141, v[100:103]
	ds_write_b128 v147, v[80:83]
	s_waitcnt lgkmcnt(2)
	global_store_dwordx4 v[72:73], v[88:91], off nt
	v_add_co_u32_e32 v72, vcc, s74, v150
	s_nop 1
	v_addc_co_u32_e32 v73, vcc, 0, v151, vcc
	global_store_dwordx4 v[72:73], v[92:95], off nt
	ds_read_b128 v[72:75], v142
	ds_read_b128 v[80:83], v148 offset:1024
	s_mov_b32 s13, 0x40000
	v_cvt_pk_bf16_f32 v68, v68, v69
	v_cvt_pk_bf16_f32 v69, v70, v71
	v_cvt_pk_bf16_f32 v70, v64, v65
	v_add_co_u32_e32 v64, vcc, s13, v150
	s_mov_b32 s13, 0x50000
	s_nop 0
	v_addc_co_u32_e32 v65, vcc, 0, v151, vcc
	v_cvt_pk_bf16_f32 v84, v84, v85
	v_cvt_pk_bf16_f32 v85, v86, v87
	v_cvt_pk_bf16_f32 v86, v76, v77
	v_cvt_pk_bf16_f32 v87, v78, v79
	v_cvt_pk_bf16_f32 v71, v66, v67
	ds_write_b128 v141, v[84:87]
	ds_write_b128 v147, v[68:71]
	s_waitcnt lgkmcnt(2)
	global_store_dwordx4 v[64:65], v[72:75], off nt
	v_add_co_u32_e32 v64, vcc, s13, v150
	s_nop 1
	v_addc_co_u32_e32 v65, vcc, 0, v151, vcc
	global_store_dwordx4 v[64:65], v[80:83], off nt
	ds_read_b128 v[64:67], v142
	ds_read_b128 v[68:71], v148 offset:1024
	s_mov_b32 s13, 0x60000
	v_cvt_pk_bf16_f32 v48, v48, v49
	v_cvt_pk_bf16_f32 v49, v50, v51
	v_cvt_pk_bf16_f32 v50, v40, v41
	v_add_co_u32_e32 v40, vcc, s13, v150
	s_mov_b32 s13, 0x70000
	s_nop 0
	v_addc_co_u32_e32 v41, vcc, 0, v151, vcc
	v_cvt_pk_bf16_f32 v60, v60, v61
	v_cvt_pk_bf16_f32 v61, v62, v63
	v_cvt_pk_bf16_f32 v62, v56, v57
	v_cvt_pk_bf16_f32 v63, v58, v59
	v_cvt_pk_bf16_f32 v51, v42, v43
	ds_write_b128 v141, v[60:63]
	ds_write_b128 v147, v[48:51]
	s_waitcnt lgkmcnt(2)
	global_store_dwordx4 v[40:41], v[64:67], off nt
	v_add_co_u32_e32 v40, vcc, s13, v150
	s_nop 1
	v_addc_co_u32_e32 v41, vcc, 0, v151, vcc
	global_store_dwordx4 v[40:41], v[68:71], off nt
	ds_read_b128 v[40:43], v142
	ds_read_b128 v[48:51], v148 offset:1024
	s_mov_b32 s13, 0x100000
	v_cvt_pk_bf16_f32 v32, v32, v33
	v_cvt_pk_bf16_f32 v33, v34, v35
	v_cvt_pk_bf16_f32 v34, v24, v25
	v_add_co_u32_e32 v24, vcc, s13, v150
	s_mov_b32 s13, 0x110000
	s_nop 0
	v_addc_co_u32_e32 v25, vcc, 0, v151, vcc
	v_cvt_pk_bf16_f32 v52, v52, v53
	v_cvt_pk_bf16_f32 v53, v54, v55
	v_cvt_pk_bf16_f32 v54, v44, v45
	v_cvt_pk_bf16_f32 v55, v46, v47
	v_cvt_pk_bf16_f32 v35, v26, v27
	ds_write_b128 v141, v[52:55]
	ds_write_b128 v147, v[32:35]
	s_waitcnt lgkmcnt(2)
	global_store_dwordx4 v[24:25], v[40:43], off nt
	v_add_co_u32_e32 v24, vcc, s13, v150
	s_nop 1
	v_addc_co_u32_e32 v25, vcc, 0, v151, vcc
	global_store_dwordx4 v[24:25], v[48:51], off nt
	ds_read_b128 v[24:27], v142
	ds_read_b128 v[32:35], v148 offset:1024
	s_mov_b32 s13, 0x120000
	v_cvt_pk_bf16_f32 v16, v16, v17
	v_cvt_pk_bf16_f32 v17, v18, v19
	v_cvt_pk_bf16_f32 v18, v8, v9
	v_add_co_u32_e32 v8, vcc, s13, v150
	s_mov_b32 s13, 0x130000
	s_nop 0
	v_addc_co_u32_e32 v9, vcc, 0, v151, vcc
	v_cvt_pk_bf16_f32 v36, v36, v37
	v_cvt_pk_bf16_f32 v37, v38, v39
	v_cvt_pk_bf16_f32 v38, v28, v29
	v_cvt_pk_bf16_f32 v39, v30, v31
	v_cvt_pk_bf16_f32 v19, v10, v11
	ds_write_b128 v141, v[36:39]
	ds_write_b128 v147, v[16:19]
	s_waitcnt lgkmcnt(2)
	global_store_dwordx4 v[8:9], v[24:27], off nt
	v_add_co_u32_e32 v8, vcc, s13, v150
	s_nop 1
	v_addc_co_u32_e32 v9, vcc, 0, v151, vcc
	global_store_dwordx4 v[8:9], v[32:35], off nt
	ds_read_b128 v[8:11], v142
	ds_read_b128 v[16:19], v148 offset:1024
	s_mov_b32 s13, 0x140000
	v_cvt_pk_bf16_f32 v4, v4, v5
	v_cvt_pk_bf16_f32 v5, v6, v7
	v_cvt_pk_bf16_f32 v6, v0, v1
	v_add_co_u32_e32 v0, vcc, s13, v150
	s_mov_b32 s13, 0x150000
	s_nop 0
	v_addc_co_u32_e32 v1, vcc, 0, v151, vcc
	v_cvt_pk_bf16_f32 v20, v20, v21
	v_cvt_pk_bf16_f32 v21, v22, v23
	v_cvt_pk_bf16_f32 v22, v12, v13
	v_cvt_pk_bf16_f32 v23, v14, v15
	v_cvt_pk_bf16_f32 v7, v2, v3
	ds_write_b128 v141, v[20:23]
	ds_write_b128 v147, v[4:7]
	s_waitcnt lgkmcnt(2)
	global_store_dwordx4 v[0:1], v[8:11], off nt
	v_add_co_u32_e32 v0, vcc, s13, v150
	s_nop 1
	v_addc_co_u32_e32 v1, vcc, 0, v151, vcc
	global_store_dwordx4 v[0:1], v[16:19], off nt
	ds_read_b128 v[0:3], v142
	ds_read_b128 v[4:7], v148 offset:1024
	v_add_co_u32_e32 v8, vcc, 0x160000, v150
	s_nop 1
	v_addc_co_u32_e32 v9, vcc, 0, v151, vcc
	s_waitcnt lgkmcnt(0)
	global_store_dwordx4 v[8:9], v[0:3], off nt
	s_nop 1
	v_add_co_u32_e32 v0, vcc, 0x170000, v150
	s_nop 1
	v_addc_co_u32_e32 v1, vcc, 0, v151, vcc
	s_andn2_b64 vcc, exec, s[6:7]
	s_mov_b64 s[6:7], -1
	global_store_dwordx4 v[0:1], v[4:7], off nt
	s_cbranch_vccnz .LBB0_850
	s_andn2_b64 vcc, exec, s[4:5]
	s_cbranch_vccnz .LBB0_849
	s_barrier
	s_branch .LBB0_849

.LBB0_910:
	v_lshl_add_u32 v150, s59, 8, v143
	v_ashrrev_i32_e32 v151, 31, v150
	s_lshl_b32 s18, s58, 8
	v_lshlrev_b64 v[150:151], 12, v[150:151]
	v_cvt_pk_bf16_f32 v124, v124, v125
	v_cvt_pk_bf16_f32 v125, v126, v127
	v_cvt_pk_bf16_f32 v126, v120, v121
	v_cvt_pk_bf16_f32 v127, v122, v123
	v_cvt_pk_bf16_f32 v108, v108, v109
	v_cvt_pk_bf16_f32 v109, v110, v111
	v_cvt_pk_bf16_f32 v110, v104, v105
	v_cvt_pk_bf16_f32 v111, v106, v107
	v_lshl_add_u64 v[150:151], s[50:51], 0, v[150:151]
	s_ashr_i32 s19, s18, 31
	ds_write_b128 v141, v[124:127]
	ds_write_b128 v147, v[108:111]
	v_lshl_add_u64 v[150:151], s[18:19], 1, v[150:151]
	ds_read_b128 v[104:107], v148 offset:1024
	ds_read_b128 v[108:111], v142
	v_lshl_add_u64 v[150:151], v[150:151], 0, s[80:81]
	v_lshl_add_u64 v[150:151], v[150:151], 0, v[160:161]
	v_cvt_pk_bf16_f32 v92, v92, v93
	v_cvt_pk_bf16_f32 v93, v94, v95
	v_cvt_pk_bf16_f32 v94, v88, v89
	v_add_co_u32_e32 v88, vcc, s97, v150
	v_cvt_pk_bf16_f32 v116, v116, v117
	v_cvt_pk_bf16_f32 v117, v118, v119
	v_cvt_pk_bf16_f32 v118, v112, v113
	v_cvt_pk_bf16_f32 v119, v114, v115
	v_cvt_pk_bf16_f32 v95, v90, v91
	v_addc_co_u32_e32 v89, vcc, 0, v151, vcc
	ds_write_b128 v141, v[116:119]
	ds_write_b128 v147, v[92:95]
	s_waitcnt lgkmcnt(0)
	global_store_dwordx4 v[150:151], v[108:111], off nt
	global_store_dwordx4 v[88:89], v[104:107], off nt
	ds_read_b128 v[88:91], v142
	ds_read_b128 v[92:95], v148 offset:1024
	v_cvt_pk_bf16_f32 v80, v80, v81
	v_cvt_pk_bf16_f32 v81, v82, v83
	v_cvt_pk_bf16_f32 v82, v72, v73
	v_add_co_u32_e32 v72, vcc, s96, v150
	s_mov_b32 s11, 0x18000
	s_nop 0
	v_addc_co_u32_e32 v73, vcc, 0, v151, vcc
	v_cvt_pk_bf16_f32 v100, v100, v101
	v_cvt_pk_bf16_f32 v101, v102, v103
	v_cvt_pk_bf16_f32 v102, v96, v97
	v_cvt_pk_bf16_f32 v103, v98, v99
	v_cvt_pk_bf16_f32 v83, v74, v75
	ds_write_b128 v141, v[100:103]
	ds_write_b128 v147, v[80:83]
	s_waitcnt lgkmcnt(2)
	global_store_dwordx4 v[72:73], v[88:91], off nt
	v_add_co_u32_e32 v72, vcc, s11, v150
	s_nop 1
	v_addc_co_u32_e32 v73, vcc, 0, v151, vcc
	global_store_dwordx4 v[72:73], v[92:95], off nt
	ds_read_b128 v[72:75], v142
	ds_read_b128 v[80:83], v148 offset:1024
	v_cvt_pk_bf16_f32 v68, v68, v69
	v_cvt_pk_bf16_f32 v69, v70, v71
	v_cvt_pk_bf16_f32 v70, v64, v65
	v_add_co_u32_e32 v64, vcc, s92, v150
	s_mov_b32 s11, 0x28000
	s_nop 0
	v_addc_co_u32_e32 v65, vcc, 0, v151, vcc
	v_cvt_pk_bf16_f32 v84, v84, v85
	v_cvt_pk_bf16_f32 v85, v86, v87
	v_cvt_pk_bf16_f32 v86, v76, v77
	v_cvt_pk_bf16_f32 v87, v78, v79
	v_cvt_pk_bf16_f32 v71, v66, v67
	ds_write_b128 v141, v[84:87]
	ds_write_b128 v147, v[68:71]
	s_waitcnt lgkmcnt(2)
	global_store_dwordx4 v[64:65], v[72:75], off nt
	v_add_co_u32_e32 v64, vcc, s11, v150
	s_nop 1
	v_addc_co_u32_e32 v65, vcc, 0, v151, vcc
	global_store_dwordx4 v[64:65], v[80:83], off nt
	ds_read_b128 v[64:67], v142
	ds_read_b128 v[68:71], v148 offset:1024
	v_cvt_pk_bf16_f32 v48, v48, v49
	v_cvt_pk_bf16_f32 v49, v50, v51
	v_cvt_pk_bf16_f32 v50, v40, v41
	v_add_co_u32_e32 v40, vcc, s74, v150
	s_mov_b32 s11, 0x38000
	s_nop 0
	v_addc_co_u32_e32 v41, vcc, 0, v151, vcc
	v_cvt_pk_bf16_f32 v60, v60, v61
	v_cvt_pk_bf16_f32 v61, v62, v63
	v_cvt_pk_bf16_f32 v62, v56, v57
	v_cvt_pk_bf16_f32 v63, v58, v59
	v_cvt_pk_bf16_f32 v51, v42, v43
	ds_write_b128 v141, v[60:63]
	ds_write_b128 v147, v[48:51]
	s_waitcnt lgkmcnt(2)
	global_store_dwordx4 v[40:41], v[64:67], off nt
	v_add_co_u32_e32 v40, vcc, s11, v150
	s_nop 1
	v_addc_co_u32_e32 v41, vcc, 0, v151, vcc
	global_store_dwordx4 v[40:41], v[68:71], off nt
	ds_read_b128 v[40:43], v142
	ds_read_b128 v[48:51], v148 offset:1024
	v_cvt_pk_bf16_f32 v32, v32, v33
	v_cvt_pk_bf16_f32 v33, v34, v35
	v_cvt_pk_bf16_f32 v34, v24, v25
	v_add_co_u32_e32 v24, vcc, s61, v150
	s_mov_b32 s11, 0x88000
	s_nop 0
	v_addc_co_u32_e32 v25, vcc, 0, v151, vcc
	v_cvt_pk_bf16_f32 v52, v52, v53
	v_cvt_pk_bf16_f32 v53, v54, v55
	v_cvt_pk_bf16_f32 v54, v44, v45
	v_cvt_pk_bf16_f32 v55, v46, v47
	v_cvt_pk_bf16_f32 v35, v26, v27
	ds_write_b128 v141, v[52:55]
	ds_write_b128 v147, v[32:35]
	s_waitcnt lgkmcnt(2)
	global_store_dwordx4 v[24:25], v[40:43], off nt
	v_add_co_u32_e32 v24, vcc, s11, v150
	s_nop 1
	v_addc_co_u32_e32 v25, vcc, 0, v151, vcc
	global_store_dwordx4 v[24:25], v[48:51], off nt
	ds_read_b128 v[24:27], v142
	ds_read_b128 v[32:35], v148 offset:1024
	v_cvt_pk_bf16_f32 v16, v16, v17
	v_cvt_pk_bf16_f32 v17, v18, v19
	v_cvt_pk_bf16_f32 v18, v8, v9
	v_add_co_u32_e32 v8, vcc, s0, v150
	s_mov_b32 s11, 0x98000
	s_nop 0
	v_addc_co_u32_e32 v9, vcc, 0, v151, vcc
	v_cvt_pk_bf16_f32 v36, v36, v37
	v_cvt_pk_bf16_f32 v37, v38, v39
	v_cvt_pk_bf16_f32 v38, v28, v29
	v_cvt_pk_bf16_f32 v39, v30, v31
	v_cvt_pk_bf16_f32 v19, v10, v11
	ds_write_b128 v141, v[36:39]
	ds_write_b128 v147, v[16:19]
	s_waitcnt lgkmcnt(2)
	global_store_dwordx4 v[8:9], v[24:27], off nt
	v_add_co_u32_e32 v8, vcc, s11, v150
	s_nop 1
	v_addc_co_u32_e32 v9, vcc, 0, v151, vcc
	global_store_dwordx4 v[8:9], v[32:35], off nt
	ds_read_b128 v[8:11], v142
	ds_read_b128 v[16:19], v148 offset:1024
	v_cvt_pk_bf16_f32 v4, v4, v5
	v_cvt_pk_bf16_f32 v5, v6, v7
	v_cvt_pk_bf16_f32 v6, v0, v1
	v_add_co_u32_e32 v0, vcc, s85, v150
	s_mov_b32 s11, 0xa8000
	s_nop 0
	v_addc_co_u32_e32 v1, vcc, 0, v151, vcc
	v_cvt_pk_bf16_f32 v20, v20, v21
	v_cvt_pk_bf16_f32 v21, v22, v23
	v_cvt_pk_bf16_f32 v22, v12, v13
	v_cvt_pk_bf16_f32 v23, v14, v15
	v_cvt_pk_bf16_f32 v7, v2, v3
	ds_write_b128 v141, v[20:23]
	ds_write_b128 v147, v[4:7]
	s_waitcnt lgkmcnt(2)
	global_store_dwordx4 v[0:1], v[8:11], off nt
	v_add_co_u32_e32 v0, vcc, s11, v150
	s_nop 1
	v_addc_co_u32_e32 v1, vcc, 0, v151, vcc
	global_store_dwordx4 v[0:1], v[16:19], off nt
	ds_read_b128 v[0:3], v142
	ds_read_b128 v[4:7], v148 offset:1024
	v_add_co_u32_e32 v8, vcc, 0xb0000, v150
	s_nop 1
	v_addc_co_u32_e32 v9, vcc, 0, v151, vcc
	s_waitcnt lgkmcnt(0)
	global_store_dwordx4 v[8:9], v[0:3], off nt
	s_nop 1
	v_add_co_u32_e32 v0, vcc, 0xb8000, v150
	s_nop 1
	v_addc_co_u32_e32 v1, vcc, 0, v151, vcc
	s_andn2_b64 vcc, exec, s[6:7]
	s_mov_b64 s[6:7], -1
	global_store_dwordx4 v[0:1], v[4:7], off nt
	s_cbranch_vccnz .LBB0_903
	s_andn2_b64 vcc, exec, s[4:5]
	s_cbranch_vccnz .LBB0_902
	s_barrier
	s_branch .LBB0_902

.LBB0_1094:
	v_lshl_add_u32 v150, s72, 8, v143
	v_ashrrev_i32_e32 v151, 31, v150
	s_lshl_b32 s30, s71, 8
	v_lshlrev_b64 v[150:151], 12, v[150:151]
	v_cvt_pk_bf16_f32 v124, v124, v125
	v_cvt_pk_bf16_f32 v125, v126, v127
	v_cvt_pk_bf16_f32 v126, v120, v121
	v_cvt_pk_bf16_f32 v127, v122, v123
	v_cvt_pk_bf16_f32 v108, v108, v109
	v_cvt_pk_bf16_f32 v109, v110, v111
	v_cvt_pk_bf16_f32 v110, v104, v105
	v_cvt_pk_bf16_f32 v111, v106, v107
	v_lshl_add_u64 v[150:151], s[52:53], 0, v[150:151]
	s_ashr_i32 s31, s30, 31
	ds_write_b128 v141, v[124:127]
	ds_write_b128 v147, v[108:111]
	v_lshl_add_u64 v[150:151], s[30:31], 1, v[150:151]
	ds_read_b128 v[104:107], v148 offset:1024
	ds_read_b128 v[108:111], v142
	v_lshl_add_u64 v[150:151], v[150:151], 0, s[80:81]
	v_lshl_add_u64 v[150:151], v[150:151], 0, v[160:161]
	v_cvt_pk_bf16_f32 v92, v92, v93
	v_cvt_pk_bf16_f32 v93, v94, v95
	v_cvt_pk_bf16_f32 v94, v88, v89
	v_add_co_u32_e32 v88, vcc, s97, v150
	v_cvt_pk_bf16_f32 v116, v116, v117
	v_cvt_pk_bf16_f32 v117, v118, v119
	v_cvt_pk_bf16_f32 v118, v112, v113
	v_cvt_pk_bf16_f32 v119, v114, v115
	v_cvt_pk_bf16_f32 v95, v90, v91
	v_addc_co_u32_e32 v89, vcc, 0, v151, vcc
	ds_write_b128 v141, v[116:119]
	ds_write_b128 v147, v[92:95]
	s_waitcnt lgkmcnt(0)
	global_store_dwordx4 v[150:151], v[108:111], off nt
	global_store_dwordx4 v[88:89], v[104:107], off nt
	ds_read_b128 v[88:91], v142
	ds_read_b128 v[92:95], v148 offset:1024
	v_cvt_pk_bf16_f32 v80, v80, v81
	v_cvt_pk_bf16_f32 v81, v82, v83
	v_cvt_pk_bf16_f32 v82, v72, v73
	v_add_co_u32_e32 v72, vcc, s96, v150
	s_mov_b32 s11, 0x18000
	s_nop 0
	v_addc_co_u32_e32 v73, vcc, 0, v151, vcc
	v_cvt_pk_bf16_f32 v100, v100, v101
	v_cvt_pk_bf16_f32 v101, v102, v103
	v_cvt_pk_bf16_f32 v102, v96, v97
	v_cvt_pk_bf16_f32 v103, v98, v99
	v_cvt_pk_bf16_f32 v83, v74, v75
	ds_write_b128 v141, v[100:103]
	ds_write_b128 v147, v[80:83]
	s_waitcnt lgkmcnt(2)
	global_store_dwordx4 v[72:73], v[88:91], off nt
	v_add_co_u32_e32 v72, vcc, s11, v150
	s_nop 1
	v_addc_co_u32_e32 v73, vcc, 0, v151, vcc
	global_store_dwordx4 v[72:73], v[92:95], off nt
	ds_read_b128 v[72:75], v142
	ds_read_b128 v[80:83], v148 offset:1024
	v_cvt_pk_bf16_f32 v68, v68, v69
	v_cvt_pk_bf16_f32 v69, v70, v71
	v_cvt_pk_bf16_f32 v70, v64, v65
	v_add_co_u32_e32 v64, vcc, s92, v150
	s_mov_b32 s11, 0x28000
	s_nop 0
	v_addc_co_u32_e32 v65, vcc, 0, v151, vcc
	v_cvt_pk_bf16_f32 v84, v84, v85
	v_cvt_pk_bf16_f32 v85, v86, v87
	v_cvt_pk_bf16_f32 v86, v76, v77
	v_cvt_pk_bf16_f32 v87, v78, v79
	v_cvt_pk_bf16_f32 v71, v66, v67
	ds_write_b128 v141, v[84:87]
	ds_write_b128 v147, v[68:71]
	s_waitcnt lgkmcnt(2)
	global_store_dwordx4 v[64:65], v[72:75], off nt
	v_add_co_u32_e32 v64, vcc, s11, v150
	s_nop 1
	v_addc_co_u32_e32 v65, vcc, 0, v151, vcc
	global_store_dwordx4 v[64:65], v[80:83], off nt
	ds_read_b128 v[64:67], v142
	ds_read_b128 v[68:71], v148 offset:1024
	v_cvt_pk_bf16_f32 v48, v48, v49
	v_cvt_pk_bf16_f32 v49, v50, v51
	v_cvt_pk_bf16_f32 v50, v40, v41
	v_add_co_u32_e32 v40, vcc, s74, v150
	s_mov_b32 s11, 0x38000
	s_nop 0
	v_addc_co_u32_e32 v41, vcc, 0, v151, vcc
	v_cvt_pk_bf16_f32 v60, v60, v61
	v_cvt_pk_bf16_f32 v61, v62, v63
	v_cvt_pk_bf16_f32 v62, v56, v57
	v_cvt_pk_bf16_f32 v63, v58, v59
	v_cvt_pk_bf16_f32 v51, v42, v43
	ds_write_b128 v141, v[60:63]
	ds_write_b128 v147, v[48:51]
	s_waitcnt lgkmcnt(2)
	global_store_dwordx4 v[40:41], v[64:67], off nt
	v_add_co_u32_e32 v40, vcc, s11, v150
	s_nop 1
	v_addc_co_u32_e32 v41, vcc, 0, v151, vcc
	global_store_dwordx4 v[40:41], v[68:71], off nt
	ds_read_b128 v[40:43], v142
	ds_read_b128 v[48:51], v148 offset:1024
	v_cvt_pk_bf16_f32 v32, v32, v33
	v_cvt_pk_bf16_f32 v33, v34, v35
	v_cvt_pk_bf16_f32 v34, v24, v25
	v_add_co_u32_e32 v24, vcc, s61, v150
	s_mov_b32 s11, 0x88000
	s_nop 0
	v_addc_co_u32_e32 v25, vcc, 0, v151, vcc
	v_cvt_pk_bf16_f32 v52, v52, v53
	v_cvt_pk_bf16_f32 v53, v54, v55
	v_cvt_pk_bf16_f32 v54, v44, v45
	v_cvt_pk_bf16_f32 v55, v46, v47
	v_cvt_pk_bf16_f32 v35, v26, v27
	ds_write_b128 v141, v[52:55]
	ds_write_b128 v147, v[32:35]
	s_waitcnt lgkmcnt(2)
	global_store_dwordx4 v[24:25], v[40:43], off nt
	v_add_co_u32_e32 v24, vcc, s11, v150
	s_nop 1
	v_addc_co_u32_e32 v25, vcc, 0, v151, vcc
	global_store_dwordx4 v[24:25], v[48:51], off nt
	ds_read_b128 v[24:27], v142
	ds_read_b128 v[32:35], v148 offset:1024
	v_cvt_pk_bf16_f32 v16, v16, v17
	v_cvt_pk_bf16_f32 v17, v18, v19
	v_cvt_pk_bf16_f32 v18, v8, v9
	v_add_co_u32_e32 v8, vcc, s0, v150
	s_mov_b32 s11, 0x98000
	s_nop 0
	v_addc_co_u32_e32 v9, vcc, 0, v151, vcc
	v_cvt_pk_bf16_f32 v36, v36, v37
	v_cvt_pk_bf16_f32 v37, v38, v39
	v_cvt_pk_bf16_f32 v38, v28, v29
	v_cvt_pk_bf16_f32 v39, v30, v31
	v_cvt_pk_bf16_f32 v19, v10, v11
	ds_write_b128 v141, v[36:39]
	ds_write_b128 v147, v[16:19]
	s_waitcnt lgkmcnt(2)
	global_store_dwordx4 v[8:9], v[24:27], off nt
	v_add_co_u32_e32 v8, vcc, s11, v150
	s_nop 1
	v_addc_co_u32_e32 v9, vcc, 0, v151, vcc
	global_store_dwordx4 v[8:9], v[32:35], off nt
	ds_read_b128 v[8:11], v142
	ds_read_b128 v[16:19], v148 offset:1024
	v_cvt_pk_bf16_f32 v4, v4, v5
	v_cvt_pk_bf16_f32 v5, v6, v7
	v_cvt_pk_bf16_f32 v6, v0, v1
	v_add_co_u32_e32 v0, vcc, s85, v150
	s_mov_b32 s11, 0xa8000
	s_nop 0
	v_addc_co_u32_e32 v1, vcc, 0, v151, vcc
	v_cvt_pk_bf16_f32 v20, v20, v21
	v_cvt_pk_bf16_f32 v21, v22, v23
	v_cvt_pk_bf16_f32 v22, v12, v13
	v_cvt_pk_bf16_f32 v23, v14, v15
	v_cvt_pk_bf16_f32 v7, v2, v3
	ds_write_b128 v141, v[20:23]
	ds_write_b128 v147, v[4:7]
	s_waitcnt lgkmcnt(2)
	global_store_dwordx4 v[0:1], v[8:11], off nt
	v_add_co_u32_e32 v0, vcc, s11, v150
	s_nop 1
	v_addc_co_u32_e32 v1, vcc, 0, v151, vcc
	global_store_dwordx4 v[0:1], v[16:19], off nt
	ds_read_b128 v[0:3], v142
	ds_read_b128 v[4:7], v148 offset:1024
	v_add_co_u32_e32 v8, vcc, 0xb0000, v150
	s_mov_b32 s90, 0x3fb8aa3b
	s_nop 0
	v_addc_co_u32_e32 v9, vcc, 0, v151, vcc
	s_waitcnt lgkmcnt(0)
	global_store_dwordx4 v[8:9], v[0:3], off nt
	s_nop 1
	v_add_co_u32_e32 v0, vcc, 0xb8000, v150
	s_nop 1
	v_addc_co_u32_e32 v1, vcc, 0, v151, vcc
	s_andn2_b64 vcc, exec, s[6:7]
	s_mov_b64 s[6:7], -1
	global_store_dwordx4 v[0:1], v[4:7], off nt
	s_cbranch_vccnz .LBB0_1087
	s_andn2_b64 vcc, exec, s[4:5]
	s_cbranch_vccnz .LBB0_1086
	s_barrier
	s_branch .LBB0_1086
